# speedup vs baseline: 1.0059x; 1.0059x over previous
.LBB0_1466:
	s_ashr_i32 s1, s10, 2
	v_lshl_or_b32 v5, s0, 5, v25
	v_lshlrev_b32_e32 v0, 3, v0
	v_lshlrev_b32_e32 v1, 3, v2
	v_lshl_or_b32 v4, s1, 5, v25
	v_mul_u32_u24_e32 v6, 0x48, v5
	v_lshlrev_b32_e32 v6, 1, v6
	v_lshlrev_b32_e32 v1, 1, v1
	v_and_b32_e32 v65, 56, v0
	v_mul_lo_u32 v0, v4, s33
	s_waitcnt lgkmcnt(0)
	s_barrier
	v_add3_u32 v88, v61, v6, v1
	s_lshl_b32 s0, s1, 12
	v_lshlrev_b32_e32 v2, 9, v2
	v_add3_u32 v89, v61, v0, v1
	v_or3_b32 v66, s0, v2, v5
	v_lshlrev_b32_e32 v160, 8, v25
	v_lshrrev_b32_e32 v161, 5, v2
	s_lshl_b32 s38, s0, 1
	v_sub_u32_e32 v162, v5, v25
	v_add3_u32 v160, v160, v161, s38
	v_lshl_add_u32 v160, v162, 1, v160
	v_add_u32_e32 v0, 0x12000, v88
	ds_read_b128 v[4:7], v89 offset:9216
	ds_read_b128 v[8:11], v0
	ds_read_b128 v[12:15], v89
	ds_read_b128 v[72:75], v89 offset:32
	ds_read_b128 v[16:19], v88 offset:36864
	ds_read_b128 v[76:79], v88 offset:36896
	v_lshl_add_u32 v2, v65, 2, v20
	s_waitcnt lgkmcnt(1)
	v_mfma_f32_32x32x16_bf16 v[20:35], v[16:19], v[12:15], 0
	ds_read_b128 v[80:83], v89 offset:9248
	v_add_u32_e32 v0, 0x12020, v88
	ds_read_b128 v[84:87], v0
	v_add_u32_e32 v0, 0x12040, v88
	v_ashrrev_i32_e32 v67, 31, v66
	s_mov_b32 s10, 0x336f8000
	s_mov_b32 s11, 0x37af8000
	v_mfma_f32_32x32x16_bf16 v[4:19], v[8:11], v[4:7], 0
	s_mov_b32 s12, 0x42828000
	s_waitcnt lgkmcnt(2)
	v_mfma_f32_32x32x16_bf16 v[20:35], v[76:79], v[72:75], v[20:35]
	s_waitcnt lgkmcnt(0)
	v_mfma_f32_32x32x16_bf16 v[4:19], v[84:87], v[80:83], v[4:19]
	ds_read_b128 v[72:75], v89 offset:64
	ds_read_b128 v[76:79], v89 offset:9280
	ds_read_b128 v[80:83], v88 offset:36928
	ds_read_b128 v[84:87], v0
	v_add_u32_e32 v0, 0x12060, v88
	s_waitcnt lgkmcnt(1)
	v_mfma_f32_32x32x16_bf16 v[20:35], v[80:83], v[72:75], v[20:35]
	s_waitcnt lgkmcnt(0)
	v_mfma_f32_32x32x16_bf16 v[4:19], v[84:87], v[76:79], v[4:19]
	ds_read_b128 v[72:75], v89 offset:96
	ds_read_b128 v[76:79], v89 offset:9312
	ds_read_b128 v[80:83], v88 offset:36960
	ds_read_b128 v[84:87], v0
	s_waitcnt lgkmcnt(1)
	v_mfma_f32_32x32x16_bf16 v[20:35], v[80:83], v[72:75], v[20:35]
	s_waitcnt lgkmcnt(0)
	v_mfma_f32_32x32x16_bf16 v[4:19], v[84:87], v[76:79], v[4:19]
	s_nop 11
	s_add_u32 s0, s46, s56
	s_addc_u32 s1, s47, s57
	s_add_u32 s38, s0, 0x336f8000
	s_addc_u32 s39, s1, 0
	s_add_u32 s40, s0, 0x37af8000
	s_addc_u32 s41, s1, 0
	v_cvt_pk_bf16_f32 v20, -v20, -v21
	v_cvt_pk_bf16_f32 v21, -v22, -v23
	v_cvt_pk_bf16_f32 v22, -v24, -v25
	v_cvt_pk_bf16_f32 v23, -v26, -v27
	v_cvt_pk_bf16_f32 v24, -v28, -v29
	v_cvt_pk_bf16_f32 v25, -v30, -v31
	v_cvt_pk_bf16_f32 v26, -v32, -v33
	v_cvt_pk_bf16_f32 v27, -v34, -v35
	v_cvt_pk_bf16_f32 v4, v4, v5
	v_cvt_pk_bf16_f32 v5, v6, v7
	v_permlane32_swap_b32_e32 v20, v22
	v_permlane32_swap_b32_e32 v21, v23
	v_permlane32_swap_b32_e32 v24, v26
	v_permlane32_swap_b32_e32 v25, v27
	global_store_dwordx4 v160, v[20:23], s[38:39]
	global_store_dwordx4 v160, v[24:27], s[38:39] offset:32
	v_cvt_pk_bf16_f32 v6, v8, v9
	v_cvt_pk_bf16_f32 v7, v10, v11
	v_cvt_pk_bf16_f32 v8, v12, v13
	v_cvt_pk_bf16_f32 v9, v14, v15
	v_cvt_pk_bf16_f32 v10, v16, v17
	v_cvt_pk_bf16_f32 v11, v18, v19
	s_nop 1
	v_permlane32_swap_b32_e32 v4, v6
	v_permlane32_swap_b32_e32 v5, v7
	v_permlane32_swap_b32_e32 v8, v10
	v_permlane32_swap_b32_e32 v9, v11
	global_store_dwordx4 v160, v[4:7], s[40:41]
	global_store_dwordx4 v160, v[8:11], s[40:41] offset:32
	s_nop 1
	v_lshl_add_u32 v0, v65, 1, v61
	v_mad_u64_u32 v[62:63], s[2:3], v60, s33, v[0:1]
	ds_read_b128 v[4:7], v2
	ds_read_b128 v[8:11], v2 offset:16
	ds_read_b128 v[12:15], v62 offset:36864
	v_and_b32_e32 v18, 0x70, v64
	s_waitcnt lgkmcnt(0)
	v_lshlrev_b32_e32 v16, 16, v12
	v_and_b32_e32 v17, 0xffff0000, v12
	v_pk_mul_f32 v[16:17], v[4:5], v[16:17]
	s_nop 0
	v_cvt_pk_bf16_f32 v12, v16, v17
	v_lshlrev_b32_e32 v16, 16, v13
	v_and_b32_e32 v17, 0xffff0000, v13
	v_pk_mul_f32 v[16:17], v[6:7], v[16:17]
	s_nop 0
	v_cvt_pk_bf16_f32 v13, v16, v17
	v_lshlrev_b32_e32 v16, 16, v14
	v_and_b32_e32 v17, 0xffff0000, v14
	v_pk_mul_f32 v[16:17], v[8:9], v[16:17]
	s_nop 0
	v_cvt_pk_bf16_f32 v14, v16, v17
	v_lshlrev_b32_e32 v16, 16, v15
	v_and_b32_e32 v17, 0xffff0000, v15
	v_pk_mul_f32 v[16:17], v[10:11], v[16:17]
	s_nop 0
	v_cvt_pk_bf16_f32 v15, v16, v17
	v_lshlrev_b32_e32 v16, 6, v60
	v_ashrrev_i32_e32 v17, 31, v16
	v_lshlrev_b64 v[16:17], 1, v[16:17]
	v_or_b32_e32 v16, v16, v18
	v_lshl_add_u64 v[64:65], s[0:1], 0, v[16:17]
	v_add_co_u32_e32 v16, vcc, s12, v64
	v_mad_u64_u32 v[60:61], s[2:3], v71, s33, v[0:1]
	s_nop 0
	v_addc_co_u32_e32 v17, vcc, 0, v65, vcc
	global_store_dwordx4 v[16:17], v[12:15], off
	ds_read_b128 v[12:15], v60 offset:36864
	v_add_u32_e32 v61, 0x16820, v88
	s_waitcnt lgkmcnt(0)
	v_lshlrev_b32_e32 v0, 16, v12
	v_and_b32_e32 v1, 0xffff0000, v12
	v_pk_mul_f32 v[0:1], v[4:5], v[0:1]
	s_nop 0
	v_cvt_pk_bf16_f32 v4, v0, v1
	v_lshlrev_b32_e32 v0, 16, v13
	v_and_b32_e32 v1, 0xffff0000, v13
	v_pk_mul_f32 v[0:1], v[6:7], v[0:1]
	s_nop 0
	v_cvt_pk_bf16_f32 v5, v0, v1
	v_lshlrev_b32_e32 v0, 16, v14
	v_and_b32_e32 v1, 0xffff0000, v14
	v_pk_mul_f32 v[0:1], v[8:9], v[0:1]
	s_nop 0
	v_cvt_pk_bf16_f32 v6, v0, v1
	v_lshlrev_b32_e32 v0, 16, v15
	v_and_b32_e32 v1, 0xffff0000, v15
	v_pk_mul_f32 v[0:1], v[10:11], v[0:1]
	s_nop 0
	v_cvt_pk_bf16_f32 v7, v0, v1
	v_lshlrev_b32_e32 v0, 6, v71
	v_ashrrev_i32_e32 v1, 31, v0
	v_lshlrev_b64 v[0:1], 1, v[0:1]
	v_or_b32_e32 v0, v0, v18
	v_lshl_add_u64 v[0:1], s[0:1], 0, v[0:1]
	v_add_co_u32_e32 v8, vcc, s12, v0
	s_nop 1
	v_addc_co_u32_e32 v9, vcc, 0, v1, vcc
	global_store_dwordx4 v[8:9], v[4:7], off
	v_add_u32_e32 v8, 0x16800, v88
	ds_read_b128 v[4:7], v89 offset:27648
	ds_read_b128 v[8:11], v8
	ds_read_b128 v[12:15], v89 offset:18432
	ds_read_b128 v[72:75], v89 offset:18464
	ds_read_b128 v[16:19], v88 offset:55296
	ds_read_b128 v[76:79], v88 offset:55328
	s_waitcnt lgkmcnt(1)
	v_mfma_f32_32x32x16_bf16 v[20:35], v[16:19], v[12:15], 0
	ds_read_b128 v[80:83], v89 offset:27680
	ds_read_b128 v[84:87], v61
	v_add_u32_e32 v61, 0x16840, v88
	v_mfma_f32_32x32x16_bf16 v[4:19], v[8:11], v[4:7], 0
	s_waitcnt lgkmcnt(2)
	v_mfma_f32_32x32x16_bf16 v[20:35], v[76:79], v[72:75], v[20:35]
	s_waitcnt lgkmcnt(0)
	v_mfma_f32_32x32x16_bf16 v[4:19], v[84:87], v[80:83], v[4:19]
	ds_read_b128 v[72:75], v89 offset:18496
	ds_read_b128 v[76:79], v89 offset:27712
	ds_read_b128 v[80:83], v88 offset:55360
	ds_read_b128 v[84:87], v61
	v_add_u32_e32 v61, 0x16860, v88
	s_waitcnt lgkmcnt(1)
	v_mfma_f32_32x32x16_bf16 v[20:35], v[80:83], v[72:75], v[20:35]
	s_waitcnt lgkmcnt(0)
	v_mfma_f32_32x32x16_bf16 v[4:19], v[84:87], v[76:79], v[4:19]
	ds_read_b128 v[72:75], v89 offset:18528
	ds_read_b128 v[76:79], v89 offset:27744
	ds_read_b128 v[80:83], v88 offset:55392
	ds_read_b128 v[84:87], v61
	s_waitcnt lgkmcnt(1)
	v_mfma_f32_32x32x16_bf16 v[20:35], v[80:83], v[72:75], v[20:35]
	s_waitcnt lgkmcnt(0)
	v_mfma_f32_32x32x16_bf16 v[4:19], v[84:87], v[76:79], v[4:19]
	s_nop 11
	s_add_u32 s38, s38, 0x4000
	s_addc_u32 s39, s39, 0
	s_add_u32 s40, s40, 0x4000
	s_addc_u32 s41, s41, 0
	v_cvt_pk_bf16_f32 v20, -v20, -v21
	v_cvt_pk_bf16_f32 v21, -v22, -v23
	v_cvt_pk_bf16_f32 v22, -v24, -v25
	v_cvt_pk_bf16_f32 v23, -v26, -v27
	v_cvt_pk_bf16_f32 v24, -v28, -v29
	v_cvt_pk_bf16_f32 v25, -v30, -v31
	v_cvt_pk_bf16_f32 v26, -v32, -v33
	v_cvt_pk_bf16_f32 v27, -v34, -v35
	v_cvt_pk_bf16_f32 v4, v4, v5
	v_cvt_pk_bf16_f32 v5, v6, v7
	v_permlane32_swap_b32_e32 v20, v22
	v_permlane32_swap_b32_e32 v21, v23
	v_permlane32_swap_b32_e32 v24, v26
	v_permlane32_swap_b32_e32 v25, v27
	global_store_dwordx4 v160, v[20:23], s[38:39]
	global_store_dwordx4 v160, v[24:27], s[38:39] offset:32
	v_cvt_pk_bf16_f32 v6, v8, v9
	v_cvt_pk_bf16_f32 v7, v10, v11
	v_cvt_pk_bf16_f32 v8, v12, v13
	v_cvt_pk_bf16_f32 v9, v14, v15
	v_cvt_pk_bf16_f32 v10, v16, v17
	v_cvt_pk_bf16_f32 v11, v18, v19
	s_nop 1
	v_permlane32_swap_b32_e32 v4, v6
	v_permlane32_swap_b32_e32 v5, v7
	v_permlane32_swap_b32_e32 v8, v10
	v_permlane32_swap_b32_e32 v9, v11
	global_store_dwordx4 v160, v[4:7], s[40:41]
	global_store_dwordx4 v160, v[8:11], s[40:41] offset:32
	s_nop 1
	ds_read_b128 v[8:11], v2 offset:256
	ds_read_b128 v[4:7], v2 offset:272
	ds_read_b128 v[12:15], v62 offset:55296
	s_mov_b32 s0, 0x4282c000
	s_waitcnt lgkmcnt(0)
	v_lshlrev_b32_e32 v16, 16, v12
	v_and_b32_e32 v17, 0xffff0000, v12
	v_pk_mul_f32 v[16:17], v[8:9], v[16:17]
	s_nop 0
	v_cvt_pk_bf16_f32 v12, v16, v17
	v_lshlrev_b32_e32 v16, 16, v13
	v_and_b32_e32 v17, 0xffff0000, v13
	v_pk_mul_f32 v[16:17], v[10:11], v[16:17]
	s_nop 0
	v_cvt_pk_bf16_f32 v13, v16, v17
	v_lshlrev_b32_e32 v16, 16, v14
	v_and_b32_e32 v17, 0xffff0000, v14
	v_pk_mul_f32 v[16:17], v[4:5], v[16:17]
	s_nop 0
	v_cvt_pk_bf16_f32 v14, v16, v17
	v_lshlrev_b32_e32 v16, 16, v15
	v_and_b32_e32 v17, 0xffff0000, v15
	v_pk_mul_f32 v[16:17], v[6:7], v[16:17]
	s_nop 0
	v_cvt_pk_bf16_f32 v15, v16, v17
	v_add_co_u32_e32 v16, vcc, s0, v64
	s_nop 1
	v_addc_co_u32_e32 v17, vcc, 0, v65, vcc
	global_store_dwordx4 v[16:17], v[12:15], off
	ds_read_b128 v[12:15], v60 offset:55296
	v_add_co_u32_e32 v0, vcc, s0, v0
	s_mul_i32 s0, s74, 0x600
	s_add_u32 s9, s9, s0
	s_waitcnt lgkmcnt(0)
	v_lshlrev_b32_e32 v16, 16, v12
	v_and_b32_e32 v17, 0xffff0000, v12
	v_lshlrev_b32_e32 v12, 16, v13
	v_and_b32_e32 v13, 0xffff0000, v13
	v_pk_mul_f32 v[8:9], v[8:9], v[16:17]
	v_pk_mul_f32 v[10:11], v[10:11], v[12:13]
	v_cvt_pk_bf16_f32 v8, v8, v9
	v_cvt_pk_bf16_f32 v9, v10, v11
	v_lshlrev_b32_e32 v10, 16, v14
	v_and_b32_e32 v11, 0xffff0000, v14
	v_pk_mul_f32 v[4:5], v[4:5], v[10:11]
	s_mul_hi_i32 s0, s74, 0x600
	v_cvt_pk_bf16_f32 v10, v4, v5
	v_lshlrev_b32_e32 v4, 16, v15
	v_and_b32_e32 v5, 0xffff0000, v15
	v_pk_mul_f32 v[4:5], v[6:7], v[4:5]
	v_addc_co_u32_e32 v1, vcc, 0, v1, vcc
	v_cvt_pk_bf16_f32 v11, v4, v5
	s_addc_u32 s8, s8, s0
	v_readlane_b32 s0, v255, 22
	global_store_dwordx4 v[0:1], v[8:11], off
	v_readlane_b32 s1, v255, 23
	s_add_u32 s56, s56, s0
	s_waitcnt lgkmcnt(0)
	s_barrier
	s_addc_u32 s57, s57, s1
	v_readlane_b32 s0, v255, 24
	v_readlane_b32 s1, v255, 25
	s_add_u32 s58, s58, s0
	s_addc_u32 s59, s59, s1
	s_andn2_b64 vcc, exec, s[60:61]
	s_cbranch_vccz .LBB0_1576
